# expert-weight conversion loop in phase A: source tile fetched with 8 global_load_dwordx4 per item instead of 32 global_load_dword (same LDS image, 32 ds_write_b32)
# speedup vs baseline: 1.0081x; 1.0081x over previous
; #define LAS __attribute__((address_space(3)))
; #define GAS __attribute__((address_space(1)))
; template <class RowFn>
; __device__ __forceinline__ void tr_item8(const float* W, int ldw, int k0, int n0, unsigned char* dst, int ldd, RowFn rf, float scale, LAS float* scr, int lane) {
;     float tv[32];
;     const GAS float* wp = (const GAS float*)(W + (size_t)(k0 + (lane >> 5)) * ldw + n0 + (lane & 31));
; #pragma unroll
;     for (int i = 0; i < 32; ++i) tv[i] = __builtin_nontemporal_load(wp + (size_t)(2 * i) * ldw);
; #pragma unroll
;     for (int i = 0; i < 32; ++i) scr[(2 * i + (lane >> 5)) * 33 + (lane & 31)] = tv[i];
; __device__ __forceinline__ void p_expert_weights(Frame& F, int l, int it0, int it1, int nw, int w) {
;     ...
;     for (int it = it0 + w; it < it1; it += nw) {
;         const int e = it / PER_E; int r = it % PER_E;
;         unsigned char* d1 = (unsigned char*)(F.ws + WS_EXP1) + (size_t)e * 512 * DM; unsigned char* d2 = (unsigned char*)(F.ws + WS_EXP2) + (size_t)e * DM * EH;
;         if (r < 2 * I1) { const int up = r >= I1; if (up) r -= I1; const int kb = r / 8, nb = r % 8;
;             const float* src = e < NEXP ? F.in[up ? I_WEU : I_WEG] + ((size_t)l * NEXP + e) * DM * EH : F.in[up ? I_WSU : I_WSG] + (size_t)l * DM * EH;
;             tr_item8(src, EH, kb * 64, nb * 32, d1, DM, RowGU{up}, up ? WEXP_SCALE * 0.6931471805599453f : WEXP_SCALE * 1.4426950408889634f, scr, F.lane); }
.LBB0_270:
	s_add_i32 s0, s4, 0xff80
	s_and_b64 s[18:19], s[36:37], exec
	s_cselect_b32 s0, s0, s4
	s_sext_i32_i16 s4, s0
	s_bfe_u32 s4, s4, 0x3001c
	s_add_i32 s4, s0, s4
	s_sext_i32_i16 s18, s4
	s_and_b32 s4, s4, 0xfff8
	s_sub_i32 s0, s0, s4
	s_lshl_b64 s[4:5], s[42:43], 19
	s_add_u32 s42, s50, s4
	s_addc_u32 s43, s51, s5
	s_lshl_b32 s4, s18, 3
	s_and_b32 s44, s4, 0xffffffc0
	v_add_u32_e32 v0, s44, v7
	s_sext_i32_i16 s0, s0
	v_ashrrev_i32_e32 v1, 31, v0
	s_lshl_b32 s46, s0, 5
	v_lshlrev_b64 v[0:1], 10, v[0:1]
	v_lshl_add_u64 v[0:1], s[48:49], 0, v[0:1]
	s_ashr_i32 s47, s46, 31
	v_lshl_add_u64 v[0:1], s[46:47], 2, v[0:1]
	v_lshl_add_u64 v[0:1], v[0:1], 0, v[192:193]
	v_lshrrev_b32_e32 v56, 3, v6
	v_sub_u32_e32 v56, v56, v7
	v_and_b32_e32 v57, 7, v6
	v_lshlrev_b32_e32 v57, 4, v57
	v_sub_u32_e32 v57, v57, v192
	v_lshl_add_u32 v54, v56, 10, v57
	v_ashrrev_i32_e32 v55, 31, v54
	v_lshl_add_u64 v[0:1], v[0:1], 0, v[54:55]
	v_mul_u32_u24_e32 v56, 0x84, v56
	v_add3_u32 v56, v10, v56, v57
	s_mov_b64 s[84:85], 0x2000
	global_load_dwordx4 v[22:25], v[0:1], off nt
	v_lshl_add_u64 v[58:59], v[0:1], 0, s[84:85]
	global_load_dwordx4 v[26:29], v[58:59], off nt
	v_lshl_add_u64 v[60:61], v[58:59], 0, s[84:85]
	global_load_dwordx4 v[30:33], v[60:61], off nt
	v_lshl_add_u64 v[62:63], v[60:61], 0, s[84:85]
	global_load_dwordx4 v[34:37], v[62:63], off nt
	v_lshl_add_u64 v[64:65], v[62:63], 0, s[84:85]
	global_load_dwordx4 v[38:41], v[64:65], off nt
	v_lshl_add_u64 v[66:67], v[64:65], 0, s[84:85]
	global_load_dwordx4 v[42:45], v[66:67], off nt
	v_lshl_add_u64 v[68:69], v[66:67], 0, s[84:85]
	global_load_dwordx4 v[46:49], v[68:69], off nt
	v_lshl_add_u64 v[70:71], v[68:69], 0, s[84:85]
	global_load_dwordx4 v[50:53], v[70:71], off nt
	s_and_b64 s[4:5], s[36:37], exec
	s_cselect_b32 s0, 0x80, 0
	s_ashr_i32 s45, s44, 31
	s_waitcnt vmcnt(0)
	ds_write_b32 v56, v22
	ds_write_b32 v56, v23 offset:4
	ds_write_b32 v56, v24 offset:8
	ds_write_b32 v56, v25 offset:12
	ds_write_b32 v56, v26 offset:1056
	ds_write_b32 v56, v27 offset:1060
	ds_write_b32 v56, v28 offset:1064
	ds_write_b32 v56, v29 offset:1068
	ds_write_b32 v56, v30 offset:2112
	ds_write_b32 v56, v31 offset:2116
	ds_write_b32 v56, v32 offset:2120
	ds_write_b32 v56, v33 offset:2124
	ds_write_b32 v56, v34 offset:3168
	ds_write_b32 v56, v35 offset:3172
	ds_write_b32 v56, v36 offset:3176
	ds_write_b32 v56, v37 offset:3180
	ds_write_b32 v56, v38 offset:4224
	ds_write_b32 v56, v39 offset:4228
	ds_write_b32 v56, v40 offset:4232
	ds_write_b32 v56, v41 offset:4236
	ds_write_b32 v56, v42 offset:5280
	ds_write_b32 v56, v43 offset:5284
	ds_write_b32 v56, v44 offset:5288
	ds_write_b32 v56, v45 offset:5292
	ds_write_b32 v56, v46 offset:6336
	ds_write_b32 v56, v47 offset:6340
	ds_write_b32 v56, v48 offset:6344
	ds_write_b32 v56, v49 offset:6348
	ds_write_b32 v56, v50 offset:7392
	ds_write_b32 v56, v51 offset:7396
	ds_write_b32 v56, v52 offset:7400
	ds_write_b32 v56, v53 offset:7404
	s_waitcnt lgkmcnt(0)
	ds_read2_b32 v[0:1], v9 offset1:33
	v_mov_b32_e32 v2, 0x4238aa3b
	v_cndmask_b32_e64 v21, v2, v233, s[36:37]
	ds_read2_b32 v[2:3], v9 offset0:66 offset1:99
	ds_read2_b32 v[22:23], v9 offset0:132 offset1:165
	s_waitcnt lgkmcnt(2)
	v_mul_f32_e32 v24, v21, v0
	v_mul_f32_e32 v1, v21, v1
	v_mov_b32_e32 v0, v193
	v_cvt_pk_fp8_f32 v0, v24, v1
	s_waitcnt lgkmcnt(1)
	v_mul_f32_e32 v24, v21, v2
	v_mul_f32_e32 v25, v21, v3
	s_waitcnt lgkmcnt(0)
	v_mul_f32_e32 v22, v21, v22
	v_mul_f32_e32 v23, v21, v23
	ds_read2_b32 v[2:3], v9 offset0:198 offset1:231
	v_mov_b32_e32 v1, v193
	v_cvt_pk_fp8_f32 v1, v22, v23
	ds_read2_b32 v[22:23], v18 offset0:8 offset1:41
	v_cvt_pk_fp8_f32 v0, v24, v25 op_sel:[0,0,1]
	s_waitcnt lgkmcnt(1)
	v_mul_f32_e32 v2, v21, v2
	v_mul_f32_e32 v3, v21, v3
	v_cvt_pk_fp8_f32 v1, v2, v3 op_sel:[0,0,1]
	s_waitcnt lgkmcnt(0)
	v_mul_f32_e32 v3, v21, v22
	ds_read2_b32 v[24:25], v18 offset0:74 offset1:107
	v_mul_f32_e32 v26, v21, v23
	ds_read2_b32 v[22:23], v18 offset0:140 offset1:173
	v_mov_b32_e32 v2, v193
	v_cvt_pk_fp8_f32 v2, v3, v26
	s_waitcnt lgkmcnt(1)
	v_mul_f32_e32 v26, v21, v24
	v_mul_f32_e32 v27, v21, v25
	s_waitcnt lgkmcnt(0)
	v_mul_f32_e32 v24, v21, v22
	v_mul_f32_e32 v25, v21, v23
	ds_read2_b32 v[22:23], v18 offset0:206 offset1:239
	v_mov_b32_e32 v3, v193
	v_cvt_pk_fp8_f32 v3, v24, v25
	ds_read2_b32 v[24:25], v19 offset0:16 offset1:49
	v_cvt_pk_fp8_f32 v2, v26, v27 op_sel:[0,0,1]
	s_waitcnt lgkmcnt(1)
	v_mul_f32_e32 v22, v21, v22
	v_mul_f32_e32 v23, v21, v23
	v_cvt_pk_fp8_f32 v3, v22, v23 op_sel:[0,0,1]
	s_waitcnt lgkmcnt(0)
	v_mul_f32_e32 v23, v21, v24
	ds_read2_b32 v[26:27], v19 offset0:82 offset1:115
	v_mul_f32_e32 v28, v21, v25
	ds_read2_b32 v[24:25], v19 offset0:148 offset1:181
	v_mov_b32_e32 v22, v193
	v_cvt_pk_fp8_f32 v22, v23, v28
	s_waitcnt lgkmcnt(1)
	v_mul_f32_e32 v28, v21, v26
	v_mul_f32_e32 v29, v21, v27
	s_waitcnt lgkmcnt(0)
	v_mul_f32_e32 v26, v21, v24
	v_mul_f32_e32 v27, v21, v25
	ds_read2_b32 v[24:25], v19 offset0:214 offset1:247
	v_mov_b32_e32 v23, v193
	v_cvt_pk_fp8_f32 v23, v26, v27
	ds_read2_b32 v[26:27], v20 offset0:24 offset1:57
	v_cvt_pk_fp8_f32 v22, v28, v29 op_sel:[0,0,1]
	s_waitcnt lgkmcnt(1)
	v_mul_f32_e32 v24, v21, v24
	v_mul_f32_e32 v25, v21, v25
	ds_read2_b32 v[28:29], v20 offset0:90 offset1:123
	v_cvt_pk_fp8_f32 v23, v24, v25 op_sel:[0,0,1]
	s_waitcnt lgkmcnt(1)
	v_mul_f32_e32 v25, v21, v26
	v_mul_f32_e32 v30, v21, v27
	ds_read2_b32 v[26:27], v20 offset0:156 offset1:189
	v_mov_b32_e32 v24, v193
	v_cvt_pk_fp8_f32 v24, v25, v30
	s_waitcnt lgkmcnt(1)
	v_mul_f32_e32 v30, v21, v28
	v_mul_f32_e32 v31, v21, v29
	ds_read2_b32 v[28:29], v20 offset0:222 offset1:255
	s_waitcnt lgkmcnt(1)
	v_mul_f32_e32 v26, v21, v26
	v_mul_f32_e32 v27, v21, v27
	v_mov_b32_e32 v25, v193
	v_cvt_pk_fp8_f32 v25, v26, v27
	s_waitcnt lgkmcnt(0)
	v_mul_f32_e32 v26, v21, v28
	v_mul_f32_e32 v21, v21, v29
	v_cvt_pk_fp8_f32 v24, v30, v31 op_sel:[0,0,1]
	v_cvt_pk_fp8_f32 v25, v26, v21 op_sel:[0,0,1]
	v_add_u32_e32 v21, s46, v8
	v_lshlrev_b32_e32 v26, 1, v21
	v_and_b32_e32 v26, 0xffffff00, v26
	v_and_b32_e32 v21, 0x7f, v21
	v_or3_b32 v26, v21, s0, v26
	v_ashrrev_i32_e32 v27, 31, v26
	v_lshlrev_b64 v[26:27], 10, v[26:27]
	v_lshl_add_u64 v[26:27], s[42:43], 0, v[26:27]
	v_lshl_add_u64 v[26:27], v[26:27], 0, s[44:45]
	v_lshl_add_u64 v[26:27], v[26:27], 0, v[4:5]
	global_store_dwordx4 v[26:27], v[0:3], off
	global_store_dwordx4 v[26:27], v[22:25], off offset:16
	s_waitcnt lgkmcnt(0)

; #define LAS __attribute__((address_space(3)))
; #define GAS __attribute__((address_space(1)))
; template <class RowFn>
; __device__ __forceinline__ void tr_item8(const float* W, int ldw, int k0, int n0, unsigned char* dst, int ldd, RowFn rf, float scale, LAS float* scr, int lane) {
;     float tv[32];
;     const GAS float* wp = (const GAS float*)(W + (size_t)(k0 + (lane >> 5)) * ldw + n0 + (lane & 31));
; #pragma unroll
;     for (int i = 0; i < 32; ++i) tv[i] = __builtin_nontemporal_load(wp + (size_t)(2 * i) * ldw);
; #pragma unroll
;     for (int i = 0; i < 32; ++i) scr[(2 * i + (lane >> 5)) * 33 + (lane & 31)] = tv[i];
; __device__ __forceinline__ void p_expert_weights(Frame& F, int l, int it0, int it1, int nw, int w) {
;     ...
;         else { r -= 2 * I1; const int kb = r / 32, nb = r % 32;
;             const float* src = e < NEXP ? F.in[I_WED] + ((size_t)l * NEXP + e) * EH * DM : F.in[I_WSD] + (size_t)l * EH * DM;
;             tr_item8(src, DM, kb * 64, nb * 32, d2, EH, RowId{}, WEXP_SCALE, scr, F.lane); }
.LBB0_272:
	s_mul_hi_i32 s0, s21, 0x2aaaaaab
	s_lshr_b32 s4, s0, 31
	s_ashr_i32 s0, s0, 6
	s_add_i32 s42, s0, s4
	s_mul_i32 s0, s42, 0xfffffe80
	s_add_i32 s4, s21, s0
	s_ashr_i32 s43, s42, 31
	s_cmpk_gt_i32 s4, 0xff
	s_mov_b64 s[36:37], -1
	s_cbranch_scc0 .LBB0_274
	s_lshl_b64 s[18:19], s[42:43], 18
	s_add_u32 s36, s52, s18
	s_addc_u32 s37, s53, s19
	s_lshl_b64 s[18:19], s[42:43], 20
	s_add_u32 s0, s54, s18
	s_addc_u32 s5, s55, s19
	s_cmp_lt_i32 s21, 0xc000
	s_cselect_b32 s18, s0, s56
	s_mul_i32 s0, s42, 0xfffffd00
	s_cselect_b32 s19, s5, s57
	s_add_i32 s0, s60, s0
	s_and_b32 s0, s0, 0x7fffffc0
	s_add_i32 s44, s0, 0xfffffe00
	v_add_u32_e32 v0, s44, v7
	v_ashrrev_i32_e32 v1, 31, v0
	s_and_b32 s5, s58, 0x3e0
	v_lshlrev_b64 v[0:1], 12, v[0:1]
	v_lshl_add_u64 v[0:1], s[18:19], 0, v[0:1]
	s_lshl_b32 s22, s5, 2
	v_lshl_add_u64 v[0:1], v[0:1], 0, s[22:23]
	v_lshl_add_u64 v[0:1], v[0:1], 0, v[192:193]
	v_lshrrev_b32_e32 v56, 3, v6
	v_sub_u32_e32 v56, v56, v7
	v_and_b32_e32 v57, 7, v6
	v_lshlrev_b32_e32 v57, 4, v57
	v_sub_u32_e32 v57, v57, v192
	v_lshl_add_u32 v54, v56, 12, v57
	v_ashrrev_i32_e32 v55, 31, v54
	v_lshl_add_u64 v[0:1], v[0:1], 0, v[54:55]
	v_mul_u32_u24_e32 v56, 0x84, v56
	v_add3_u32 v56, v10, v56, v57
	s_mov_b64 s[84:85], 0x8000
	global_load_dwordx4 v[22:25], v[0:1], off nt
	v_lshl_add_u64 v[58:59], v[0:1], 0, s[84:85]
	global_load_dwordx4 v[26:29], v[58:59], off nt
	v_lshl_add_u64 v[60:61], v[58:59], 0, s[84:85]
	global_load_dwordx4 v[30:33], v[60:61], off nt
	v_lshl_add_u64 v[62:63], v[60:61], 0, s[84:85]
	global_load_dwordx4 v[34:37], v[62:63], off nt
	v_lshl_add_u64 v[64:65], v[62:63], 0, s[84:85]
	global_load_dwordx4 v[38:41], v[64:65], off nt
	v_lshl_add_u64 v[66:67], v[64:65], 0, s[84:85]
	global_load_dwordx4 v[42:45], v[66:67], off nt
	v_lshl_add_u64 v[68:69], v[66:67], 0, s[84:85]
	global_load_dwordx4 v[46:49], v[68:69], off nt
	v_lshl_add_u64 v[70:71], v[68:69], 0, s[84:85]
	global_load_dwordx4 v[50:53], v[70:71], off nt
	s_mov_b32 s45, s23
	s_waitcnt vmcnt(0)
	ds_write_b32 v56, v22
	ds_write_b32 v56, v23 offset:4
	ds_write_b32 v56, v24 offset:8
	ds_write_b32 v56, v25 offset:12
	ds_write_b32 v56, v26 offset:1056
	ds_write_b32 v56, v27 offset:1060
	ds_write_b32 v56, v28 offset:1064
	ds_write_b32 v56, v29 offset:1068
	ds_write_b32 v56, v30 offset:2112
	ds_write_b32 v56, v31 offset:2116
	ds_write_b32 v56, v32 offset:2120
	ds_write_b32 v56, v33 offset:2124
	ds_write_b32 v56, v34 offset:3168
	ds_write_b32 v56, v35 offset:3172
	ds_write_b32 v56, v36 offset:3176
	ds_write_b32 v56, v37 offset:3180
	ds_write_b32 v56, v38 offset:4224
	ds_write_b32 v56, v39 offset:4228
	ds_write_b32 v56, v40 offset:4232
	ds_write_b32 v56, v41 offset:4236
	ds_write_b32 v56, v42 offset:5280
	ds_write_b32 v56, v43 offset:5284
	ds_write_b32 v56, v44 offset:5288
	ds_write_b32 v56, v45 offset:5292
	ds_write_b32 v56, v46 offset:6336
	ds_write_b32 v56, v47 offset:6340
	ds_write_b32 v56, v48 offset:6344
	ds_write_b32 v56, v49 offset:6348
	ds_write_b32 v56, v50 offset:7392
	ds_write_b32 v56, v51 offset:7396
	ds_write_b32 v56, v52 offset:7400
	ds_write_b32 v56, v53 offset:7404
	s_waitcnt lgkmcnt(0)
	ds_read2_b32 v[0:1], v9 offset1:33
	ds_read2_b32 v[22:23], v18 offset0:74 offset1:107
	ds_read2_b32 v[24:25], v19 offset0:82 offset1:115
	ds_read2_b32 v[26:27], v20 offset0:90 offset1:123
	s_waitcnt lgkmcnt(3)
	v_mul_f32_e32 v2, 0x42000000, v0
	v_mul_f32_e32 v1, 0x42000000, v1
	v_mov_b32_e32 v0, v193
	v_cvt_pk_fp8_f32 v0, v2, v1
	ds_read2_b32 v[2:3], v9 offset0:66 offset1:99
	s_waitcnt lgkmcnt(0)
	v_mul_f32_e32 v1, 0x42000000, v2
	v_mul_f32_e32 v2, 0x42000000, v3
	v_cvt_pk_fp8_f32 v0, v1, v2 op_sel:[0,0,1]
	ds_read2_b32 v[2:3], v9 offset0:132 offset1:165
	v_mov_b32_e32 v1, v193
	s_waitcnt lgkmcnt(0)
	v_mul_f32_e32 v2, 0x42000000, v2
	v_mul_f32_e32 v3, 0x42000000, v3
	v_cvt_pk_fp8_f32 v1, v2, v3
	ds_read2_b32 v[2:3], v9 offset0:198 offset1:231
	s_waitcnt lgkmcnt(0)
	v_mul_f32_e32 v2, 0x42000000, v2
	v_mul_f32_e32 v3, 0x42000000, v3
	v_cvt_pk_fp8_f32 v1, v2, v3 op_sel:[0,0,1]
	ds_read2_b32 v[2:3], v18 offset0:8 offset1:41
	s_waitcnt lgkmcnt(0)
	v_mul_f32_e32 v21, 0x42000000, v2
	v_mul_f32_e32 v3, 0x42000000, v3
	v_mov_b32_e32 v2, v193
	v_cvt_pk_fp8_f32 v2, v21, v3
	v_mul_f32_e32 v3, 0x42000000, v22
	v_mul_f32_e32 v21, 0x42000000, v23
	ds_read2_b32 v[22:23], v18 offset0:140 offset1:173
	v_cvt_pk_fp8_f32 v2, v3, v21 op_sel:[0,0,1]
	v_mov_b32_e32 v3, v193
	s_waitcnt lgkmcnt(0)
	v_mul_f32_e32 v21, 0x42000000, v22
	v_mul_f32_e32 v22, 0x42000000, v23
	v_cvt_pk_fp8_f32 v3, v21, v22
	ds_read2_b32 v[22:23], v18 offset0:206 offset1:239
	s_waitcnt lgkmcnt(0)
	v_mul_f32_e32 v21, 0x42000000, v22
	v_mul_f32_e32 v22, 0x42000000, v23
	v_cvt_pk_fp8_f32 v3, v21, v22 op_sel:[0,0,1]
	ds_read2_b32 v[22:23], v19 offset0:16 offset1:49
	s_waitcnt lgkmcnt(0)
	v_mul_f32_e32 v21, 0x42000000, v22
	v_mul_f32_e32 v23, 0x42000000, v23
	v_mov_b32_e32 v22, v193
	v_cvt_pk_fp8_f32 v22, v21, v23
	v_mul_f32_e32 v21, 0x42000000, v24
	v_mul_f32_e32 v23, 0x42000000, v25
	ds_read2_b32 v[24:25], v19 offset0:148 offset1:181
	v_cvt_pk_fp8_f32 v22, v21, v23 op_sel:[0,0,1]
	v_mov_b32_e32 v23, v193
	s_waitcnt lgkmcnt(0)
	v_mul_f32_e32 v21, 0x42000000, v24
	v_mul_f32_e32 v24, 0x42000000, v25
	v_cvt_pk_fp8_f32 v23, v21, v24
	ds_read2_b32 v[24:25], v19 offset0:214 offset1:247
	s_waitcnt lgkmcnt(0)
	v_mul_f32_e32 v21, 0x42000000, v24
	v_mul_f32_e32 v24, 0x42000000, v25
	v_cvt_pk_fp8_f32 v23, v21, v24 op_sel:[0,0,1]
	ds_read2_b32 v[24:25], v20 offset0:24 offset1:57
	s_waitcnt lgkmcnt(0)
	v_mul_f32_e32 v21, 0x42000000, v24
	v_mul_f32_e32 v25, 0x42000000, v25
	v_mov_b32_e32 v24, v193
	v_cvt_pk_fp8_f32 v24, v21, v25
	v_mul_f32_e32 v21, 0x42000000, v26
	v_mul_f32_e32 v25, 0x42000000, v27
	ds_read2_b32 v[26:27], v20 offset0:156 offset1:189
	v_cvt_pk_fp8_f32 v24, v21, v25 op_sel:[0,0,1]
	v_mov_b32_e32 v25, v193
	s_waitcnt lgkmcnt(0)
	v_mul_f32_e32 v21, 0x42000000, v26
	v_mul_f32_e32 v26, 0x42000000, v27
	v_cvt_pk_fp8_f32 v25, v21, v26
	ds_read2_b32 v[26:27], v20 offset0:222 offset1:255
	s_waitcnt lgkmcnt(0)
	v_mul_f32_e32 v21, 0x42000000, v26
	v_mul_f32_e32 v26, 0x42000000, v27
	v_cvt_pk_fp8_f32 v25, v21, v26 op_sel:[0,0,1]
	v_add_u32_e32 v26, s5, v8
	v_ashrrev_i32_e32 v27, 31, v26
	v_lshlrev_b64 v[26:27], 8, v[26:27]
	v_lshl_add_u64 v[26:27], s[36:37], 0, v[26:27]
	v_lshl_add_u64 v[26:27], v[26:27], 0, s[44:45]
	v_lshl_add_u64 v[26:27], v[26:27], 0, v[4:5]
	global_store_dwordx4 v[26:27], v[0:3], off
	global_store_dwordx4 v[26:27], v[22:25], off offset:16
	s_waitcnt lgkmcnt(0)
	s_mov_b64 s[36:37], 0
